# P1: alignment barrier of the leading wave group deferred to the head of the epilogue (its unit-scheduling code runs under the other group's last MFMA interval)
# speedup vs baseline: 1.0152x; 1.0080x over previous
; #define PG8_BAR __builtin_amdgcn_s_barrier()
;     __device__ __forceinline__ bool next(int i, pg8::Unit& u) const { const int L = i * G + c; if (L >= nM * 4) return false; int pm, pn; pg8::tile_remap<4>(L, nM, pm, pn); if (rev) pm = nM - 1 - pm; u.pm = pm; u.pn = pn; u.aux = 0; u.skip = 0; return true; }
;     __device__ __forceinline__ bool next(int i, pg8::Unit& u) const { const int L = first + i * stride; if (i >= nmine || L >= 512) return false; u.pm = L & 3; u.pn = (L >> 2) & 3; u.aux = L >> 4; u.skip = 0; return true; }
;     __device__ __forceinline__ bool next(int i, pg8::Unit& u) const { if (!TW) { const bool r = Base::next(i, u); u.skip = 0; return r; } const bool r = Base::next(i >> 1, u); u.skip = !(i & 1); return r; }
; template <class Epi, class Sched, bool F8 = false, bool PF = false, bool I8 = false, int PID = -1>
; __device__ __forceinline__ void gemm_phase(LAS unsigned char* lds, LAS unsigned char* xlds, const int RP, const int RPB, const int nt, const Sched& S, const Epi& E, const int stagger_ticks) {
;     ...
;         if (wr == 0) PG8_BAR;
;         Unit nn; bool has_nn = false; unsigned gv[4] = {vA0, vA1, vA2, vA3};
;         if (has_next) { has_nn = S.next(ui + 2, nn); if (Sched::GATHER) { if (has_nn) S.a_offsets(nn, Rr, Cc, RP, gv); } }
.LBB0_216:
.LBB0_218:
	v_cndmask_b32_e64 v46, 0, 1, s[20:21]
	v_cmp_ne_u32_e64 s[0:1], 1, v46
	s_andn2_b64 vcc, exec, s[20:21]
	s_cbranch_vccnz .LBB0_225
	s_add_i32 s2, s9, 2
	s_mul_i32 s46, s2, s92
	s_add_i32 s46, s46, s33
	s_cmpk_gt_i32 s46, 0xaff
	s_mov_b64 s[20:21], 0
	s_cbranch_scc1 .LBB0_226
	s_cmpk_gt_i32 s46, 0x9ff
	s_mov_b64 s[2:3], -1
	s_cbranch_scc0 .LBB0_222
	s_add_i32 s2, s46, 0xfffff600
	s_lshr_b32 s22, s2, 3
	s_and_b32 s18, s46, 7
	s_mov_b64 s[2:3], 0

; #define LAS __attribute__((address_space(3)))
;     __device__ __forceinline__ void operator()(const f32x4 (&acc)[2][2][4][2], const pg8::Unit& u, int wr, int wc, int fr, int fq) const {
;         const int row0 = u.pm * 256 + wr * 64 + fr, col0 = u.pn * 256 + wc * 64 + 16 * fq;
;         size_t bo = WS_PROJ; int ld = NP; if (u.aux == 1) { bo = WS_KM; ld = 2 * D; }
;         bf16* base = (bf16*)(ws + bo);
;         const bool act = (u.aux == 0 && u.pn >= 6);
;         f32x4 cb[2][2]; float ra[2][4];
;         { const LAS float* sb = (const LAS float*)(btab + u.par * 2048) + wc * 64 + 16 * fq; const LAS float* sa = (const LAS float*)(btab + u.par * 2048 + 1024) + wr * 64 + fr;
; #pragma unroll
;           for (int bj = 0; bj < 2; ++bj) { cb[bj][0] = *(const LAS f32x4*)(sb + bj * 8); cb[bj][1] = *(const LAS f32x4*)(sb + bj * 8 + 4); }
; #pragma unroll
;           for (int ai = 0; ai < 2; ++ai)
; #pragma unroll
;               for (int m = 0; m < 4; ++m) ra[ai][m] = sa[ai * 128 + m * 16]; }
;     ...
;         float nss = 0.f;
; #pragma unroll
;         for (int ai = 0; ai < 2; ++ai)
; #pragma unroll
;             for (int bj = 0; bj < 2; ++bj)
; #pragma unroll
;                 for (int m = 0; m < 4; ++m)
; #pragma unroll
;                     for (int n = 0; n < 2; ++n) { const f32x4 a = acc[ai][bj][m][n]; nss += (a[0] * a[0] + a[1] * a[1]) + (a[2] * a[2] + a[3] * a[3]); }
;         const float nsc = sqrtf(nss * (1.0f / 128.0f)) * (NOISE_PROBE * 0.0001f * 3.4641016f) * (1.0f / 16777216.0f);
;     ...
; #pragma unroll
;         for (int ai = 0; ai < 2; ++ai)
; #pragma unroll
;             for (int m = 0; m < 4; ++m) { bf16* rowp = base + (size_t)(row0 + ai * 128 + m * 16) * ld + col0;
; #pragma unroll
;                 for (int bj = 0; bj < 2; ++bj) { f32x4 v0 = __builtin_convertvector(__builtin_bit_cast(pg8::i32x4, acc[ai][bj][m][0]), f32x4) * (cb[bj][0] * ra[ai][m]), v1 = __builtin_convertvector(__builtin_bit_cast(pg8::i32x4, acc[ai][bj][m][1]), f32x4) * (cb[bj][1] * ra[ai][m]);
;     ...
;                     { const unsigned idx0 = (unsigned)((row0 + ai * 128 + m * 16) * 4096 + col0 + bj * 8) + (u.aux ? 0x40000000u : 0u);
; #pragma unroll
;                       for (int j = 0; j < 8; ++j) { unsigned h = (idx0 + j) * 0x9E3779B1u; h ^= h >> 15; h *= 0x85EBCA77u; h ^= h >> 13; h *= 0xC2B2AE3Du; h ^= h >> 16;
.LBB0_225:
	s_mov_b64 s[20:21], 0
.LBB0_226:
	s_and_b64 vcc, exec, s[42:43]
	s_cbranch_vccz .Lmy_nobar2
	s_barrier
.Lmy_nobar2:
	s_cmp_gt_i32 s74, 5
	s_cselect_b64 s[2:3], -1, 0
	s_add_i32 s46, s75, 0
	v_mov_b32_e32 v46, v0
	s_add_i32 s46, s46, 0x22800
	s_lshl_b32 s47, s66, 2
	s_add_i32 s47, s46, s47
	v_and_b32_e32 v159, 48, v46
	v_and_b32_e32 v158, 15, v46
	v_lshl_add_u32 v46, v159, 2, s47
	s_lshl_b32 s47, s64, 2
	s_add_i32 s48, s46, s47
	v_lshl_add_u32 v146, v158, 2, s48
	v_add_u32_e32 v146, 0x400, v146
	v_cvt_f32_i32_e32 v155, v143
	v_cvt_f32_i32_e32 v145, v145
	v_cvt_f32_i32_e32 v144, v144
	v_cvt_f32_i32_e32 v154, v142
	ds_read_b128 v[66:69], v46
	ds_read_b128 v[58:61], v46 offset:16
	ds_read_b128 v[54:57], v46 offset:32
	ds_read_b128 v[46:49], v46 offset:48
	ds_read2_b32 v[152:153], v146 offset1:16
	ds_read2_b32 v[150:151], v146 offset0:32 offset1:48
	ds_read2_b32 v[148:149], v146 offset0:128 offset1:144
	ds_read2_b32 v[146:147], v146 offset0:160 offset1:176
	v_cvt_f32_i32_e32 v141, v141
	v_cvt_f32_i32_e32 v140, v140
	s_cmp_eq_u32 s19, 0
	v_cvt_f32_i32_e32 v139, v139
	v_cvt_f32_i32_e32 v138, v138
	s_cselect_b64 s[46:47], -1, 0
	s_waitcnt lgkmcnt(3)
	v_pk_mul_f32 v[156:157], v[66:67], v[152:153] op_sel_hi:[1,0]
	v_pk_mul_f32 v[142:143], v[68:69], v[152:153] op_sel_hi:[1,0]
	s_and_b64 s[46:47], s[46:47], s[2:3]
	v_pk_mul_f32 v[142:143], v[142:143], v[144:145]
	v_pk_mul_f32 v[144:145], v[156:157], v[154:155]
	v_pk_mul_f32 v[154:155], v[60:61], v[152:153] op_sel_hi:[1,0]
	v_pk_mul_f32 v[156:157], v[58:59], v[152:153] op_sel_hi:[1,0]
	v_pk_mul_f32 v[154:155], v[154:155], v[140:141]
	v_cndmask_b32_e64 v140, 0, 1, s[46:47]
	v_cmp_ne_u32_e64 s[2:3], 1, v140
	s_andn2_b64 vcc, exec, s[46:47]
	v_pk_mul_f32 v[156:157], v[156:157], v[138:139]
	s_cbranch_vccnz .LBB0_228
	v_pk_mul_f32 v[140:141], v[144:145], v[144:145]
	v_pk_mul_f32 v[138:139], v[142:143], v[142:143]
	v_pk_fma_f32 v[140:141], v[140:141], s[8:9], 1.0 op_sel_hi:[1,0,0]
	v_pk_fma_f32 v[138:139], v[138:139], s[8:9], 1.0 op_sel_hi:[1,0,0]
	v_pk_mul_f32 v[140:141], v[144:145], v[140:141]
	v_pk_mul_f32 v[138:139], v[142:143], v[138:139]
	v_pk_mul_f32 v[140:141], v[140:141], s[44:45] op_sel_hi:[1,0]
	v_pk_mul_f32 v[138:139], v[138:139], s[44:45] op_sel_hi:[1,0]
	v_min_f32_e32 v140, 0x42700000, v140
	v_min_f32_e32 v141, 0x42700000, v141
	v_exp_f32_e32 v140, v140
	v_exp_f32_e32 v141, v141
	v_min_f32_e32 v138, 0x42700000, v138
	v_min_f32_e32 v139, 0x42700000, v139
	v_exp_f32_e32 v138, v138
	v_exp_f32_e32 v139, v139
	v_pk_add_f32 v[140:141], v[140:141], 1.0 op_sel_hi:[1,0]
	v_pk_add_f32 v[138:139], v[138:139], 1.0 op_sel_hi:[1,0]
	v_mul_f32_e32 v160, v140, v141
	v_rcp_f32_e32 v160, v160
	v_mul_f32_e32 v161, v138, v139
	v_rcp_f32_e32 v162, v161
	v_pk_mul_f32 v[140:141], v[140:141], v[160:161] op_sel:[1,0] op_sel_hi:[0,0]
	v_pk_mul_f32 v[160:161], v[156:157], v[156:157]
	v_pk_mul_f32 v[144:145], v[144:145], v[140:141]
	v_pk_mul_f32 v[140:141], v[154:155], v[154:155]
	v_pk_fma_f32 v[160:161], v[160:161], s[8:9], 1.0 op_sel_hi:[1,0,0]
	v_pk_fma_f32 v[140:141], v[140:141], s[8:9], 1.0 op_sel_hi:[1,0,0]
	v_pk_mul_f32 v[160:161], v[156:157], v[160:161]
	v_pk_mul_f32 v[140:141], v[154:155], v[140:141]
	v_pk_mul_f32 v[160:161], v[160:161], s[44:45] op_sel_hi:[1,0]
	v_pk_mul_f32 v[140:141], v[140:141], s[44:45] op_sel_hi:[1,0]
	v_min_f32_e32 v160, 0x42700000, v160
	v_min_f32_e32 v161, 0x42700000, v161
	v_exp_f32_e32 v160, v160
	v_exp_f32_e32 v161, v161
	v_min_f32_e32 v140, 0x42700000, v140
	v_min_f32_e32 v141, 0x42700000, v141
	v_exp_f32_e32 v140, v140
	v_exp_f32_e32 v141, v141
	v_pk_add_f32 v[160:161], v[160:161], 1.0 op_sel_hi:[1,0]
	v_pk_mul_f32 v[138:139], v[138:139], v[162:163] op_sel:[1,0] op_sel_hi:[0,0]
	v_mul_f32_e32 v162, v160, v161
	v_pk_add_f32 v[140:141], v[140:141], 1.0 op_sel_hi:[1,0]
	v_rcp_f32_e32 v162, v162
	v_mul_f32_e32 v163, v140, v141
	v_rcp_f32_e32 v164, v163
	v_pk_mul_f32 v[142:143], v[142:143], v[138:139]
	v_pk_mul_f32 v[138:139], v[160:161], v[162:163] op_sel:[1,0] op_sel_hi:[0,0]
	v_pk_mul_f32 v[156:157], v[156:157], v[138:139]
	v_pk_mul_f32 v[138:139], v[140:141], v[164:165] op_sel:[1,0] op_sel_hi:[0,0]
	v_pk_mul_f32 v[154:155], v[154:155], v[138:139]
